# diff-attention row sums: packed adds on two independent pair accumulators (no back-to-back dependent pk ops)
# baseline (speedup 1.0000x reference)
; #define WAIT_BAR(N) asm volatile("s_waitcnt vmcnt(" #N ") lgkmcnt(0)\n\ts_barrier":::"memory")
;   #define DMA_V(t,slot) glds16(vsrc+(long)(t)*KVBLK*PQ,(unsigned)__builtin_amdgcn_readfirstlane(vdst+(slot)))
;   #define CMASK(P0,P1,t) do{int jb_=(t)-(NT-4); if(jb_>=0)cmask(P0,P1,jb_,qrel,hi);}while(0)
;   #define ROT() do{sl_prev=sl_cur;sl_cur=sl_next;sl_next=(sl_next==(NSLOT-1)*SLOTB)?0:sl_next+SLOTB;}while(0)
;   #define PKW(P,B) cvtpk_s(P[B],P[B+1])
;   #define CMASK(P0,P1,t) do{}while(0)
;   #define CMASK(P0,P1,t) do{int jb_=(t)-(NT-4); if(jb_>=0)cmask(P0,P1,jb_,qrel,hi);}while(0)
; #define WAIT_BAR(N) asm volatile("s_waitcnt vmcnt(" #N ") lgkmcnt(0)\n\ts_barrier":::"memory")
;   #define DMA_V(t,slot) do{ glds16(vsrc+(long)(t)*KVBLK*PQ,(unsigned)__builtin_amdgcn_readfirstlane(vdst+2*(slot))); glds16(vsrc+(long)(t)*KVBLK*PQ+64,(unsigned)__builtin_amdgcn_readfirstlane(vdst+2*(slot)+8192)); }while(0)
;   #define CMASK(P0,P1,t) do{int jb_=(t)-(NT-4); if(jb_>=0)cmask(P0,P1,jb_,qrel,hi);}while(0)
;   #define ROT() do{sl_prev=sl_cur;sl_cur=sl_next;sl_next=(sl_next==(NSLOT-1)*SLOTB)?0:sl_next+SLOTB;}while(0)
;   #define PKW(P,B) cvtpk_s(P[B],P[B+1])
; template<int THRL> __device__ __forceinline__ void attn_unit2(int b,int qb,const bf16*Q,const bf16*__restrict__ K,const bf16*__restrict__ V,bf16*O,char*shm,int tid_in){
;     ...
;   WAIT_BAR(4);
;   qkt(c0,c1,Kbase,qr,zero16,r32,hi);asm volatile("s_nop 15\n\ts_nop 7":"+v"(c0),"+v"(c1));CMASK(c0,c1,0);
;   { const float rm=rowmax(c0,c1); mhat=rm;
;     _Pragma("unroll") for(int r=0;r<16;++r){c0[r]=__builtin_amdgcn_exp2f(c0[r]-rm);c1[r]=__builtin_amdgcn_exp2f(c1[r]-rm);}
;     float sacc=c0[0]+c0[1]; _Pragma("unroll") for(int r=2;r<16;++r)sacc+=c0[r]; _Pragma("unroll") for(int r=0;r<16;++r)sacc+=c1[r]; l_reg=sacc;
;     pa0=(u32x4){PKW(c0,0),PKW(c0,2),PKW(c0,4),PKW(c0,6)};pa1=(u32x4){PKW(c0,8),PKW(c0,10),PKW(c0,12),PKW(c0,14)};pa2=(u32x4){PKW(c1,0),PKW(c1,2),PKW(c1,4),PKW(c1,6)};pa3=(u32x4){PKW(c1,8),PKW(c1,10),PKW(c1,12),PKW(c1,14)}; }
;   WAIT_BAR(0);
;   DMA_V(1,SLOTB);
;   ROT();
;   kfa[0]=*(const __attribute__((address_space(3))) bf16x8*)(kp0+sl_cur);      kfa[1]=*(const __attribute__((address_space(3))) bf16x8*)(kp0+sl_cur+512);
;   kfa[2]=*(const __attribute__((address_space(3))) bf16x8*)(kp0+sl_cur+2048); kfa[3]=*(const __attribute__((address_space(3))) bf16x8*)(kp0+sl_cur+2560);
;   WAIT_BAR(2);
.LBB0_563:
	v_lshlrev_b32_e32 v37, 1, v3
	v_and_b32_e32 v37, 32, v37
	v_lshlrev_b32_e32 v38, 4, v3
	v_add3_u32 v36, 0, v37, v36
	v_lshlrev_b32_e32 v37, 8, v228
	v_and_b32_e32 v38, 0xc0, v38
	v_add3_u32 v225, v36, v37, v38
	v_max3_f32 v36, v4, v5, v20
	v_max3_f32 v37, v6, v7, v21
	s_and_b32 s9, s8, 0x3fffffc0
	v_max3_f32 v36, v36, v22, v23
	v_max3_f32 v37, v37, v10, v11
	s_lshl_b32 s9, s9, 2
	v_max3_f32 v36, v36, v8, v9
	v_max3_f32 v37, v37, v26, v27
	s_add_i32 s10, s22, 0x100
	v_max3_f32 v36, v36, v24, v25
	v_max3_f32 v37, v37, v14, v15
	s_add_i32 s17, s9, 0
	v_max3_f32 v36, v36, v12, v13
	v_max3_f32 v37, v37, v30, v31
	s_add_i32 s17, s17, 0x12000
	v_max3_f32 v36, v36, v28, v29
	v_max3_f32 v37, v37, v18, v19
	s_lshr_b32 s20, s10, 6
	v_max3_f32 v36, v36, v16, v17
	v_max3_f32 v37, v37, v34, v35
	s_cmp_lg_u32 0, -1
	v_max3_f32 v36, v36, v32, v33
	s_cselect_b32 s9, 0, 0
	v_max_f32_e32 v36, v36, v37
	s_waitcnt vmcnt(0) lgkmcnt(0)
	s_barrier
	s_mov_b64 s[10:11], 0x90000
	v_mov_b32_e32 v37, v36
	s_nop 1
	v_permlane32_swap_b32_e32 v36, v37
	v_max_f32_e32 v206, v36, v37
	s_add_i32 s3, s9, s3
	v_sub_f32_e32 v4, v4, v206
	v_sub_f32_e32 v5, v5, v206
	v_exp_f32_e32 v4, v4
	v_exp_f32_e32 v5, v5
	v_sub_f32_e32 v6, v6, v206
	v_exp_f32_e32 v6, v6
	v_sub_f32_e32 v7, v7, v206
	v_exp_f32_e32 v7, v7
	v_sub_f32_e32 v8, v8, v206
	v_exp_f32_e32 v8, v8
	v_sub_f32_e32 v9, v9, v206
	v_exp_f32_e32 v9, v9
	v_sub_f32_e32 v10, v10, v206
	v_exp_f32_e32 v10, v10
	v_sub_f32_e32 v11, v11, v206
	v_exp_f32_e32 v11, v11
	v_sub_f32_e32 v12, v12, v206
	v_exp_f32_e32 v12, v12
	v_sub_f32_e32 v13, v13, v206
	v_exp_f32_e32 v13, v13
	v_sub_f32_e32 v14, v14, v206
	v_pk_add_f32 v[242:243], v[4:5], v[8:9]
	v_exp_f32_e32 v14, v14
	v_sub_f32_e32 v15, v15, v206
	v_exp_f32_e32 v15, v15
	v_sub_f32_e32 v16, v16, v206
	v_pk_add_f32 v[244:245], v[6:7], v[10:11]
	v_exp_f32_e32 v16, v16
	v_sub_f32_e32 v17, v17, v206
	v_exp_f32_e32 v17, v17
	v_sub_f32_e32 v18, v18, v206
	v_pk_add_f32 v[242:243], v[242:243], v[12:13]
	v_exp_f32_e32 v18, v18
	v_sub_f32_e32 v19, v19, v206
	v_sub_f32_e32 v20, v20, v206
	v_exp_f32_e32 v19, v19
	v_pk_add_f32 v[244:245], v[244:245], v[14:15]
	v_exp_f32_e32 v20, v20
	v_sub_f32_e32 v21, v21, v206
	v_exp_f32_e32 v21, v21
	v_sub_f32_e32 v22, v22, v206
	v_pk_add_f32 v[242:243], v[242:243], v[16:17]
	v_exp_f32_e32 v22, v22
	v_sub_f32_e32 v23, v23, v206
	v_exp_f32_e32 v23, v23
	v_sub_f32_e32 v24, v24, v206
	v_pk_add_f32 v[244:245], v[244:245], v[18:19]
	v_exp_f32_e32 v24, v24
	v_sub_f32_e32 v25, v25, v206
	v_exp_f32_e32 v25, v25
	v_sub_f32_e32 v26, v26, v206
	v_pk_add_f32 v[242:243], v[242:243], v[20:21]
	v_exp_f32_e32 v26, v26
	v_sub_f32_e32 v27, v27, v206
	v_exp_f32_e32 v27, v27
	v_sub_f32_e32 v28, v28, v206
	v_pk_add_f32 v[244:245], v[244:245], v[22:23]
	v_exp_f32_e32 v28, v28
	v_sub_f32_e32 v29, v29, v206
	v_exp_f32_e32 v29, v29
	v_sub_f32_e32 v30, v30, v206
	v_pk_add_f32 v[242:243], v[242:243], v[24:25]
	v_exp_f32_e32 v30, v30
	v_sub_f32_e32 v31, v31, v206
	v_cvt_pk_bf16_f32 v142, v4, v5
	v_lshl_add_u64 v[4:5], v[0:1], 0, s[10:11]
	s_add_i32 s9, s3, 0xa000
	s_mov_b32 s10, m0
	s_mov_b32 m0, s9
	s_nop 0
	global_load_lds_dwordx4 v[4:5], off
	s_mov_b32 m0, s10
	v_exp_f32_e32 v31, v31
	v_sub_f32_e32 v32, v32, v206
	v_pk_add_f32 v[244:245], v[244:245], v[26:27]
	s_mov_b64 s[10:11], 0x90080
	v_exp_f32_e32 v32, v32
	v_sub_f32_e32 v33, v33, v206
	v_lshl_add_u64 v[0:1], v[0:1], 0, s[10:11]
	s_add_i32 s3, s3, 0xc000
	s_mov_b32 s9, m0
	s_mov_b32 m0, s3
	s_nop 0
	global_load_lds_dwordx4 v[0:1], off
	s_mov_b32 m0, s9
	v_exp_f32_e32 v33, v33
	v_sub_f32_e32 v34, v34, v206
	v_pk_add_f32 v[242:243], v[242:243], v[28:29]
	ds_read_b128 v[166:169], v224 offset:8192
	ds_read_b128 v[162:165], v224 offset:8704
	ds_read_b128 v[174:177], v224 offset:10240
	ds_read_b128 v[170:173], v224 offset:10752
	v_exp_f32_e32 v34, v34
	v_sub_f32_e32 v35, v35, v206
	v_exp_f32_e32 v35, v35
	v_pk_add_f32 v[244:245], v[244:245], v[30:31]
	v_pk_add_f32 v[242:243], v[242:243], v[32:33]
	s_waitcnt vmcnt(2) lgkmcnt(0)
	s_barrier
	v_and_b32_e32 v0, 3, v3
	s_mov_b32 s8, 1
	v_pk_add_f32 v[244:245], v[244:245], v[34:35]
	v_pk_add_f32 v[242:243], v[242:243], v[244:245]
	v_add_f32_e32 v227, v242, v243
	v_cvt_pk_bf16_f32 v143, v6, v7
	v_cvt_pk_bf16_f32 v144, v8, v9
	v_cvt_pk_bf16_f32 v145, v10, v11
	v_cvt_pk_bf16_f32 v138, v12, v13
	v_cvt_pk_bf16_f32 v139, v14, v15
	v_cvt_pk_bf16_f32 v140, v16, v17
	v_cvt_pk_bf16_f32 v141, v18, v19
	v_cvt_pk_bf16_f32 v134, v20, v21
	v_cvt_pk_bf16_f32 v135, v22, v23
	v_cvt_pk_bf16_f32 v136, v24, v25
	v_cvt_pk_bf16_f32 v137, v26, v27
	v_cvt_pk_bf16_f32 v130, v28, v29
	v_cvt_pk_bf16_f32 v131, v30, v31
	v_cvt_pk_bf16_f32 v132, v32, v33
	v_cvt_pk_bf16_f32 v133, v34, v35
	s_mov_b32 s24, 0
	s_andn2_b64 vcc, exec, s[6:7]
	v_lshlrev_b32_e32 v226, 4, v228
	s_mul_hi_i32 s25, s2, 0x1200000
	s_mul_i32 s26, s2, 0x1200000
	v_lshlrev_b32_e32 v196, 4, v0
	s_cbranch_vccnz .LBB0_579
	s_lshl_b64 s[6:7], s[4:5], 1
	s_add_u32 s6, s6, s0
	s_addc_u32 s7, s7, s1
	s_add_u32 s6, s6, s26
	v_mov_b32_e32 v197, v2
	s_addc_u32 s7, s7, s25
	v_lshl_add_u64 v[0:1], s[6:7], 0, v[196:197]
	v_mov_b32_e32 v195, v2
	v_readlane_b32 s6, v254, 27
	v_lshl_add_u64 v[0:1], v[0:1], 0, v[194:195]
	v_readlane_b32 s7, v254, 28
	v_mov_b32_e32 v14, v2
	v_mov_b32_e32 v15, v2
	v_lshl_add_u64 v[208:209], s[6:7], 0, v[0:1]
	v_mov_b32_e32 v0, v2
	v_mov_b32_e32 v1, v2
	v_mov_b32_e32 v3, v2
	v_mov_b32_e32 v4, v2
	v_mov_b32_e32 v5, v2
	v_mov_b32_e32 v6, v2
	v_mov_b32_e32 v7, v2
	v_mov_b32_e32 v8, v2
	v_mov_b32_e32 v9, v2
	v_mov_b32_e32 v10, v2
	v_mov_b32_e32 v11, v2
	v_mov_b32_e32 v12, v2
	v_mov_b32_e32 v13, v2
	v_mov_b64_e32 v[78:79], v[14:15]
	v_mov_b64_e32 v[62:63], v[14:15]
	v_mov_b64_e32 v[46:47], v[14:15]
	v_mov_b64_e32 v[30:31], v[14:15]
	v_cmp_gt_u32_e64 s[2:3], 32, v222
	v_lshl_add_u32 v229, v221, 2, s17
	s_movk_i32 s24, 0x4000
	s_movk_i32 s29, 0x2000
	s_mov_b32 s8, 0
	s_mov_b32 s28, 6
	s_mov_b64 s[6:7], 0
	v_mov_b64_e32 v[76:77], v[12:13]
	v_mov_b64_e32 v[74:75], v[10:11]
	v_mov_b64_e32 v[72:73], v[8:9]
	v_mov_b64_e32 v[70:71], v[6:7]
	v_mov_b64_e32 v[68:69], v[4:5]
	v_mov_b64_e32 v[66:67], v[2:3]
	v_mov_b64_e32 v[64:65], v[0:1]
	v_mov_b64_e32 v[60:61], v[12:13]
	v_mov_b64_e32 v[58:59], v[10:11]
	v_mov_b64_e32 v[56:57], v[8:9]
	v_mov_b64_e32 v[54:55], v[6:7]
	v_mov_b64_e32 v[52:53], v[4:5]
	v_mov_b64_e32 v[50:51], v[2:3]
	v_mov_b64_e32 v[48:49], v[0:1]
	v_mov_b64_e32 v[44:45], v[12:13]
	v_mov_b64_e32 v[42:43], v[10:11]
	v_mov_b64_e32 v[40:41], v[8:9]
	v_mov_b64_e32 v[38:39], v[6:7]
	v_mov_b64_e32 v[36:37], v[4:5]
	v_mov_b64_e32 v[34:35], v[2:3]
	v_mov_b64_e32 v[32:33], v[0:1]
	v_mov_b64_e32 v[28:29], v[12:13]
	v_mov_b64_e32 v[26:27], v[10:11]
	v_mov_b64_e32 v[24:25], v[8:9]
	v_mov_b64_e32 v[22:23], v[6:7]
	v_mov_b64_e32 v[20:21], v[4:5]
	v_mov_b64_e32 v[18:19], v[2:3]
	v_mov_b64_e32 v[16:17], v[0:1]

.LBB0_566:
	s_waitcnt lgkmcnt(14)
	v_mfma_f32_32x32x16_bf16 v[64:79], v[142:145], v[8:11], v[64:79]
	ds_read_b64_tr_b16 v[112:113], v3 offset:32768
	ds_read_b64_tr_b16 v[114:115], v3 offset:33280
	v_exp_f32_e32 v96, v96
	v_exp_f32_e32 v97, v97
	v_exp_f32_e32 v98, v98
	v_exp_f32_e32 v99, v99
	s_waitcnt lgkmcnt(14)
	v_mfma_f32_32x32x16_bf16 v[48:63], v[142:145], v[4:7], v[48:63]
	ds_read_b64_tr_b16 v[186:187], v3 offset:36864
	ds_read_b64_tr_b16 v[188:189], v3 offset:37376
	v_exp_f32_e32 v100, v100
	v_exp_f32_e32 v101, v101
	v_exp_f32_e32 v102, v102
	v_exp_f32_e32 v103, v103
	v_add_u32_e32 v192, s24, v224
	ds_read_b128 v[8:11], v192
	ds_read_b128 v[4:7], v192 offset:512
	s_waitcnt lgkmcnt(14)
	v_mfma_f32_32x32x16_bf16 v[64:79], v[138:141], v[12:15], v[64:79]
	ds_read_b64_tr_b16 v[230:231], v3 offset:33792
	ds_read_b64_tr_b16 v[232:233], v3 offset:34304
	v_exp_f32_e32 v104, v104
	v_exp_f32_e32 v105, v105
	v_exp_f32_e32 v106, v106
	v_exp_f32_e32 v107, v107
	ds_read_b128 v[162:165], v192 offset:2048
	ds_read_b128 v[12:15], v192 offset:2560
	v_mfma_f32_32x32x16_bf16 v[48:63], v[138:141], v[182:185], v[48:63]
	ds_read_b64_tr_b16 v[182:183], v3 offset:37888
	ds_read_b64_tr_b16 v[184:185], v3 offset:38400
	v_exp_f32_e32 v108, v108
	v_exp_f32_e32 v109, v109
	v_exp_f32_e32 v110, v110
	v_exp_f32_e32 v111, v111
	s_waitcnt lgkmcnt(14)
	v_mfma_f32_32x32x16_bf16 v[64:79], v[134:137], v[178:181], v[64:79]
	ds_read_b64_tr_b16 v[178:179], v3 offset:34816
	ds_read_b64_tr_b16 v[180:181], v3 offset:35328
	v_exp_f32_e32 v80, v80
	v_exp_f32_e32 v81, v81
	v_exp_f32_e32 v82, v82
	v_exp_f32_e32 v83, v83
	v_mfma_f32_32x32x16_bf16 v[48:63], v[134:137], v[174:177], v[48:63]
	ds_read_b64_tr_b16 v[174:175], v3 offset:38912
	ds_read_b64_tr_b16 v[176:177], v3 offset:39424
	v_exp_f32_e32 v84, v84
	v_exp_f32_e32 v85, v85
	v_exp_f32_e32 v86, v86
	v_exp_f32_e32 v87, v87
	v_mfma_f32_32x32x16_bf16 v[64:79], v[130:133], v[170:173], v[64:79]
	ds_read_b64_tr_b16 v[170:171], v3 offset:35840
	ds_read_b64_tr_b16 v[172:173], v3 offset:36352
	v_exp_f32_e32 v88, v88
	v_exp_f32_e32 v89, v89
	v_exp_f32_e32 v90, v90
	v_exp_f32_e32 v91, v91
	s_waitcnt lgkmcnt(14)
	v_mfma_f32_32x32x16_bf16 v[48:63], v[130:133], v[166:169], v[48:63]
	ds_read_b64_tr_b16 v[166:167], v3 offset:39936
	ds_read_b64_tr_b16 v[168:169], v3 offset:40448
	v_exp_f32_e32 v92, v92
	v_exp_f32_e32 v93, v93
	v_exp_f32_e32 v94, v94
	v_exp_f32_e32 v95, v95
	v_mfma_f32_32x32x16_bf16 v[32:47], v[142:145], v[112:115], v[32:47]
	v_pk_add_f32 v[242:243], v[96:97], v[100:101]
	v_cvt_pk_bf16_f32 v126, v96, v97
	v_cvt_pk_bf16_f32 v127, v98, v99
	v_mfma_f32_32x32x16_bf16 v[16:31], v[142:145], v[186:189], v[16:31]
	v_pk_add_f32 v[244:245], v[98:99], v[102:103]
	v_pk_add_f32 v[242:243], v[242:243], v[104:105]
	v_cvt_pk_bf16_f32 v128, v100, v101
	v_cvt_pk_bf16_f32 v129, v102, v103
	s_waitcnt lgkmcnt(12)
	v_mfma_f32_32x32x16_bf16 v[32:47], v[138:141], v[230:233], v[32:47]
	v_pk_add_f32 v[244:245], v[244:245], v[106:107]
	v_pk_add_f32 v[242:243], v[242:243], v[108:109]
	v_cvt_pk_bf16_f32 v122, v104, v105
	v_cvt_pk_bf16_f32 v123, v106, v107
	s_waitcnt lgkmcnt(8)
	v_mfma_f32_32x32x16_bf16 v[16:31], v[138:141], v[182:185], v[16:31]
	v_pk_add_f32 v[244:245], v[244:245], v[110:111]
	v_pk_add_f32 v[242:243], v[242:243], v[80:81]
	v_cvt_pk_bf16_f32 v124, v108, v109
	v_cvt_pk_bf16_f32 v125, v110, v111
	s_waitcnt lgkmcnt(6)
	v_mfma_f32_32x32x16_bf16 v[32:47], v[134:137], v[178:181], v[32:47]
	v_pk_add_f32 v[244:245], v[244:245], v[82:83]
	v_pk_add_f32 v[242:243], v[242:243], v[84:85]
	v_cvt_pk_bf16_f32 v118, v80, v81
	v_cvt_pk_bf16_f32 v119, v82, v83
	s_waitcnt lgkmcnt(4)
	v_mfma_f32_32x32x16_bf16 v[16:31], v[134:137], v[174:177], v[16:31]
	v_pk_add_f32 v[244:245], v[244:245], v[86:87]
	v_pk_add_f32 v[242:243], v[242:243], v[88:89]
	v_cvt_pk_bf16_f32 v120, v84, v85
	v_cvt_pk_bf16_f32 v121, v86, v87
	s_waitcnt lgkmcnt(2)
	v_mfma_f32_32x32x16_bf16 v[32:47], v[130:133], v[170:173], v[32:47]
	v_pk_add_f32 v[244:245], v[244:245], v[90:91]
	v_pk_add_f32 v[242:243], v[242:243], v[92:93]
	v_cvt_pk_bf16_f32 v114, v88, v89
	v_cvt_pk_bf16_f32 v115, v90, v91
	s_waitcnt lgkmcnt(0)
	v_mfma_f32_32x32x16_bf16 v[16:31], v[130:133], v[166:169], v[16:31]
	v_pk_add_f32 v[244:245], v[244:245], v[94:95]
	v_pk_add_f32 v[242:243], v[242:243], v[244:245]
	v_add_f32_e32 v3, v242, v243
	v_cvt_pk_bf16_f32 v116, v92, v93
	v_cvt_pk_bf16_f32 v117, v94, v95
	s_waitcnt vmcnt(2) lgkmcnt(0)
	s_barrier
	s_andn2_b64 vcc, exec, s[8:9]
	v_add_u32_e32 v195, s17, v226
	s_cbranch_vccnz .LBB0_568
	s_waitcnt lgkmcnt(0)
	ds_read_b128 v[80:83], v195 offset:96
	ds_read_b128 v[84:87], v195 offset:64
	ds_read_b128 v[88:91], v195 offset:32
	ds_read_b128 v[92:95], v195
	s_waitcnt lgkmcnt(3)
	v_pk_mul_f32 v[76:77], v[76:77], v[80:81]
	s_waitcnt lgkmcnt(2)
	v_pk_mul_f32 v[72:73], v[72:73], v[84:85]
	s_waitcnt lgkmcnt(1)
	v_pk_mul_f32 v[68:69], v[68:69], v[88:89]
	v_pk_mul_f32 v[78:79], v[78:79], v[82:83]
	v_pk_mul_f32 v[74:75], v[74:75], v[86:87]
	v_pk_mul_f32 v[70:71], v[70:71], v[90:91]
	s_waitcnt lgkmcnt(0)
	v_pk_mul_f32 v[66:67], v[66:67], v[94:95]
	v_pk_mul_f32 v[64:65], v[64:65], v[92:93]
	v_pk_mul_f32 v[60:61], v[60:61], v[80:81]
	v_pk_mul_f32 v[56:57], v[56:57], v[84:85]
	v_pk_mul_f32 v[52:53], v[52:53], v[88:89]
	v_pk_mul_f32 v[62:63], v[62:63], v[82:83]
	v_pk_mul_f32 v[58:59], v[58:59], v[86:87]
	v_pk_mul_f32 v[54:55], v[54:55], v[90:91]
	v_pk_mul_f32 v[50:51], v[50:51], v[94:95]
	v_pk_mul_f32 v[48:49], v[48:49], v[92:93]
	v_pk_mul_f32 v[44:45], v[44:45], v[80:81]
	v_pk_mul_f32 v[40:41], v[40:41], v[84:85]
	v_pk_mul_f32 v[36:37], v[36:37], v[88:89]
	v_pk_mul_f32 v[46:47], v[46:47], v[82:83]
	v_pk_mul_f32 v[42:43], v[42:43], v[86:87]
	v_pk_mul_f32 v[38:39], v[38:39], v[90:91]
	v_pk_mul_f32 v[34:35], v[34:35], v[94:95]
	v_pk_mul_f32 v[32:33], v[32:33], v[92:93]
	v_pk_mul_f32 v[28:29], v[28:29], v[80:81]
	v_pk_mul_f32 v[24:25], v[24:25], v[84:85]
	v_pk_mul_f32 v[20:21], v[20:21], v[88:89]
	v_pk_mul_f32 v[30:31], v[30:31], v[82:83]
	v_pk_mul_f32 v[26:27], v[26:27], v[86:87]
	v_pk_mul_f32 v[22:23], v[22:23], v[90:91]
	v_pk_mul_f32 v[18:19], v[18:19], v[94:95]
	v_pk_mul_f32 v[16:17], v[16:17], v[92:93]

.LBB0_569:
	s_waitcnt lgkmcnt(14)
	v_mfma_f32_32x32x16_bf16 v[64:79], v[126:129], v[174:177], v[64:79]
	ds_read_b64_tr_b16 v[186:187], v130 offset:32768
	ds_read_b64_tr_b16 v[188:189], v130 offset:33280
	v_exp_f32_e32 v96, v80
	v_exp_f32_e32 v97, v81
	v_exp_f32_e32 v98, v98
	v_exp_f32_e32 v99, v99
	s_waitcnt lgkmcnt(14)
	v_mfma_f32_32x32x16_bf16 v[48:63], v[126:129], v[166:169], v[48:63]
	ds_read_b64_tr_b16 v[190:191], v130 offset:36864
	ds_read_b64_tr_b16 v[192:193], v130 offset:37376
	v_exp_f32_e32 v100, v100
	v_exp_f32_e32 v101, v101
	v_exp_f32_e32 v102, v102
	v_exp_f32_e32 v103, v103
	v_add_u32_e32 v80, s27, v224
	ds_read_b128 v[166:169], v80
	ds_read_b128 v[162:165], v80 offset:512
	s_waitcnt lgkmcnt(14)
	v_mfma_f32_32x32x16_bf16 v[64:79], v[122:125], v[170:173], v[64:79]
	ds_read_b64_tr_b16 v[230:231], v130 offset:33792
	ds_read_b64_tr_b16 v[232:233], v130 offset:34304
	v_exp_f32_e32 v104, v104
	v_exp_f32_e32 v105, v105
	v_exp_f32_e32 v106, v106
	v_exp_f32_e32 v107, v107
	ds_read_b128 v[174:177], v80 offset:2048
	ds_read_b128 v[170:173], v80 offset:2560
	v_mfma_f32_32x32x16_bf16 v[48:63], v[122:125], v[182:185], v[48:63]
	ds_read_b64_tr_b16 v[182:183], v130 offset:37888
	ds_read_b64_tr_b16 v[184:185], v130 offset:38400
	v_exp_f32_e32 v108, v108
	v_exp_f32_e32 v109, v109
	v_exp_f32_e32 v110, v110
	v_exp_f32_e32 v111, v111
	s_waitcnt lgkmcnt(14)
	v_mfma_f32_32x32x16_bf16 v[64:79], v[118:121], v[178:181], v[64:79]
	ds_read_b64_tr_b16 v[178:179], v130 offset:34816
	ds_read_b64_tr_b16 v[180:181], v130 offset:35328
	v_exp_f32_e32 v80, v0
	v_exp_f32_e32 v81, v1
	v_exp_f32_e32 v82, v82
	v_exp_f32_e32 v83, v83
	v_mfma_f32_32x32x16_bf16 v[48:63], v[118:121], v[12:15], v[48:63]
	ds_read_b64_tr_b16 v[12:13], v130 offset:38912
	ds_read_b64_tr_b16 v[14:15], v130 offset:39424
	v_exp_f32_e32 v84, v84
	v_exp_f32_e32 v85, v85
	v_exp_f32_e32 v86, v86
	v_exp_f32_e32 v87, v87
	v_mfma_f32_32x32x16_bf16 v[64:79], v[114:117], v[8:11], v[64:79]
	ds_read_b64_tr_b16 v[8:9], v130 offset:35840
	ds_read_b64_tr_b16 v[10:11], v130 offset:36352
	v_exp_f32_e32 v88, v88
	v_exp_f32_e32 v89, v89
	v_exp_f32_e32 v90, v90
	v_exp_f32_e32 v91, v91
	s_waitcnt lgkmcnt(14)
	v_mfma_f32_32x32x16_bf16 v[48:63], v[114:117], v[4:7], v[48:63]
	ds_read_b64_tr_b16 v[4:5], v130 offset:39936
	ds_read_b64_tr_b16 v[6:7], v130 offset:40448
	v_exp_f32_e32 v92, v92
	v_exp_f32_e32 v93, v93
	v_exp_f32_e32 v94, v94
	v_exp_f32_e32 v95, v95
	v_mfma_f32_32x32x16_bf16 v[32:47], v[126:129], v[186:189], v[32:47]
	v_pk_add_f32 v[242:243], v[96:97], v[100:101]
	v_cvt_pk_bf16_f32 v142, v96, v97
	v_cvt_pk_bf16_f32 v143, v98, v99
	v_mfma_f32_32x32x16_bf16 v[16:31], v[126:129], v[190:193], v[16:31]
	v_pk_add_f32 v[244:245], v[98:99], v[102:103]
	v_pk_add_f32 v[242:243], v[242:243], v[104:105]
	v_cvt_pk_bf16_f32 v144, v100, v101
	v_cvt_pk_bf16_f32 v145, v102, v103
	s_waitcnt lgkmcnt(12)
	v_mfma_f32_32x32x16_bf16 v[32:47], v[122:125], v[230:233], v[32:47]
	v_pk_add_f32 v[244:245], v[244:245], v[106:107]
	v_pk_add_f32 v[242:243], v[242:243], v[108:109]
	v_cvt_pk_bf16_f32 v138, v104, v105
	v_cvt_pk_bf16_f32 v139, v106, v107
	s_waitcnt lgkmcnt(8)
	v_mfma_f32_32x32x16_bf16 v[16:31], v[122:125], v[182:185], v[16:31]
	v_pk_add_f32 v[244:245], v[244:245], v[110:111]
	v_pk_add_f32 v[242:243], v[242:243], v[80:81]
	v_cvt_pk_bf16_f32 v140, v108, v109
	v_cvt_pk_bf16_f32 v141, v110, v111
	s_waitcnt lgkmcnt(6)
	v_mfma_f32_32x32x16_bf16 v[32:47], v[118:121], v[178:181], v[32:47]
	v_pk_add_f32 v[244:245], v[244:245], v[82:83]
	v_pk_add_f32 v[242:243], v[242:243], v[84:85]
	v_cvt_pk_bf16_f32 v134, v80, v81
	v_cvt_pk_bf16_f32 v135, v82, v83
	s_waitcnt lgkmcnt(4)
	v_mfma_f32_32x32x16_bf16 v[16:31], v[118:121], v[12:15], v[16:31]
	v_pk_add_f32 v[244:245], v[244:245], v[86:87]
	v_pk_add_f32 v[242:243], v[242:243], v[88:89]
	v_cvt_pk_bf16_f32 v136, v84, v85
	v_cvt_pk_bf16_f32 v137, v86, v87
	s_waitcnt lgkmcnt(2)
	v_mfma_f32_32x32x16_bf16 v[32:47], v[114:117], v[8:11], v[32:47]
	v_pk_add_f32 v[244:245], v[244:245], v[90:91]
	v_pk_add_f32 v[242:243], v[242:243], v[92:93]
	v_cvt_pk_bf16_f32 v130, v88, v89
	v_cvt_pk_bf16_f32 v131, v90, v91
	s_waitcnt lgkmcnt(0)
	v_mfma_f32_32x32x16_bf16 v[16:31], v[114:117], v[4:7], v[16:31]
	v_pk_add_f32 v[244:245], v[244:245], v[94:95]
	v_pk_add_f32 v[242:243], v[242:243], v[244:245]
	v_add_f32_e32 v0, v242, v243
	v_cvt_pk_bf16_f32 v132, v92, v93
	v_cvt_pk_bf16_f32 v133, v94, v95
	s_waitcnt vmcnt(2) lgkmcnt(0)
	s_barrier
	s_andn2_b64 vcc, exec, s[8:9]
	s_cbranch_vccnz .LBB0_571
	s_waitcnt lgkmcnt(0)
	ds_read_b128 v[4:7], v195 offset:96
	ds_read_b128 v[8:11], v195 offset:64
	ds_read_b128 v[12:15], v195 offset:32
	ds_read_b128 v[80:83], v195
	s_waitcnt lgkmcnt(3)
	v_pk_mul_f32 v[76:77], v[76:77], v[4:5]
	s_waitcnt lgkmcnt(2)
	v_pk_mul_f32 v[72:73], v[72:73], v[8:9]
	s_waitcnt lgkmcnt(1)
	v_pk_mul_f32 v[68:69], v[68:69], v[12:13]
	v_pk_mul_f32 v[78:79], v[78:79], v[6:7]
	v_pk_mul_f32 v[74:75], v[74:75], v[10:11]
	v_pk_mul_f32 v[70:71], v[70:71], v[14:15]
	s_waitcnt lgkmcnt(0)
	v_pk_mul_f32 v[66:67], v[66:67], v[82:83]
	v_pk_mul_f32 v[64:65], v[64:65], v[80:81]
	v_pk_mul_f32 v[60:61], v[60:61], v[4:5]
	v_pk_mul_f32 v[56:57], v[56:57], v[8:9]
	v_pk_mul_f32 v[52:53], v[52:53], v[12:13]
	v_pk_mul_f32 v[62:63], v[62:63], v[6:7]
	v_pk_mul_f32 v[58:59], v[58:59], v[10:11]
	v_pk_mul_f32 v[54:55], v[54:55], v[14:15]
	v_pk_mul_f32 v[50:51], v[50:51], v[82:83]
	v_pk_mul_f32 v[48:49], v[48:49], v[80:81]
	v_pk_mul_f32 v[44:45], v[44:45], v[4:5]
	v_pk_mul_f32 v[40:41], v[40:41], v[8:9]
	v_pk_mul_f32 v[36:37], v[36:37], v[12:13]
	v_pk_mul_f32 v[46:47], v[46:47], v[6:7]
	v_pk_mul_f32 v[42:43], v[42:43], v[10:11]
	v_pk_mul_f32 v[38:39], v[38:39], v[14:15]
	v_pk_mul_f32 v[34:35], v[34:35], v[82:83]
	v_pk_mul_f32 v[32:33], v[32:33], v[80:81]
	v_pk_mul_f32 v[28:29], v[28:29], v[4:5]
	v_pk_mul_f32 v[24:25], v[24:25], v[8:9]
	v_pk_mul_f32 v[20:21], v[20:21], v[12:13]
	v_pk_mul_f32 v[30:31], v[30:31], v[6:7]
	v_pk_mul_f32 v[26:27], v[26:27], v[10:11]
	v_pk_mul_f32 v[22:23], v[22:23], v[14:15]
	v_pk_mul_f32 v[18:19], v[18:19], v[82:83]
	v_pk_mul_f32 v[16:17], v[16:17], v[80:81]

.LBB0_583:
	s_waitcnt lgkmcnt(14)
	v_mfma_f32_32x32x16_bf16 v[64:79], v[142:145], v[178:181], v[64:79]
	ds_read_b64_tr_b16 v[146:147], v0 offset:32768
	ds_read_b64_tr_b16 v[148:149], v0 offset:33280
	v_exp_f32_e32 v96, v96
	v_exp_f32_e32 v97, v97
	v_exp_f32_e32 v98, v98
	v_exp_f32_e32 v99, v99
	s_waitcnt lgkmcnt(14)
	v_mfma_f32_32x32x16_bf16 v[48:63], v[142:145], v[166:169], v[48:63]
	ds_read_b64_tr_b16 v[150:151], v0 offset:36864
	ds_read_b64_tr_b16 v[152:153], v0 offset:37376
	v_exp_f32_e32 v100, v100
	v_exp_f32_e32 v101, v101
	v_exp_f32_e32 v102, v102
	v_exp_f32_e32 v103, v103
	s_waitcnt lgkmcnt(14)
	v_mfma_f32_32x32x16_bf16 v[64:79], v[138:141], v[162:165], v[64:79]
	ds_read_b64_tr_b16 v[154:155], v0 offset:33792
	ds_read_b64_tr_b16 v[156:157], v0 offset:34304
	v_exp_f32_e32 v104, v104
	v_exp_f32_e32 v105, v105
	v_exp_f32_e32 v106, v106
	v_exp_f32_e32 v107, v107
	s_waitcnt lgkmcnt(14)
	v_mfma_f32_32x32x16_bf16 v[48:63], v[138:141], v[158:161], v[48:63]
	ds_read_b64_tr_b16 v[158:159], v0 offset:37888
	ds_read_b64_tr_b16 v[160:161], v0 offset:38400
	v_exp_f32_e32 v108, v108
	v_exp_f32_e32 v109, v109
	v_exp_f32_e32 v110, v110
	v_exp_f32_e32 v111, v111
	s_waitcnt lgkmcnt(14)
	v_mfma_f32_32x32x16_bf16 v[64:79], v[134:137], v[112:115], v[64:79]
	ds_read_b64_tr_b16 v[112:113], v0 offset:34816
	ds_read_b64_tr_b16 v[114:115], v0 offset:35328
	v_exp_f32_e32 v80, v80
	v_exp_f32_e32 v81, v81
	v_exp_f32_e32 v82, v82
	v_exp_f32_e32 v83, v83
	s_waitcnt lgkmcnt(14)
	v_mfma_f32_32x32x16_bf16 v[48:63], v[134:137], v[12:15], v[48:63]
	ds_read_b64_tr_b16 v[12:13], v0 offset:38912
	ds_read_b64_tr_b16 v[14:15], v0 offset:39424
	v_exp_f32_e32 v84, v84
	v_exp_f32_e32 v85, v85
	v_exp_f32_e32 v86, v86
	v_exp_f32_e32 v87, v87
	s_waitcnt lgkmcnt(14)
	v_mfma_f32_32x32x16_bf16 v[64:79], v[130:133], v[8:11], v[64:79]
	ds_read_b64_tr_b16 v[8:9], v0 offset:35840
	ds_read_b64_tr_b16 v[10:11], v0 offset:36352
	v_exp_f32_e32 v88, v88
	v_exp_f32_e32 v89, v89
	v_exp_f32_e32 v90, v90
	v_exp_f32_e32 v91, v91
	s_waitcnt lgkmcnt(14)
	v_mfma_f32_32x32x16_bf16 v[48:63], v[130:133], v[4:7], v[48:63]
	ds_read_b64_tr_b16 v[4:5], v0 offset:39936
	ds_read_b64_tr_b16 v[6:7], v0 offset:40448
	v_exp_f32_e32 v92, v92
	v_exp_f32_e32 v93, v93
	v_exp_f32_e32 v94, v94
	v_exp_f32_e32 v95, v95
	s_waitcnt lgkmcnt(14)
	v_mfma_f32_32x32x16_bf16 v[32:47], v[142:145], v[146:149], v[32:47]
	v_pk_add_f32 v[242:243], v[96:97], v[100:101]
	v_cvt_pk_bf16_f32 v126, v96, v97
	v_cvt_pk_bf16_f32 v127, v98, v99
	s_waitcnt lgkmcnt(12)
	v_mfma_f32_32x32x16_bf16 v[16:31], v[142:145], v[150:153], v[16:31]
	v_pk_add_f32 v[244:245], v[98:99], v[102:103]
	v_pk_add_f32 v[242:243], v[242:243], v[104:105]
	v_cvt_pk_bf16_f32 v128, v100, v101
	v_cvt_pk_bf16_f32 v129, v102, v103
	s_waitcnt lgkmcnt(10)
	v_mfma_f32_32x32x16_bf16 v[32:47], v[138:141], v[154:157], v[32:47]
	v_pk_add_f32 v[244:245], v[244:245], v[106:107]
	v_pk_add_f32 v[242:243], v[242:243], v[108:109]
	v_cvt_pk_bf16_f32 v122, v104, v105
	v_cvt_pk_bf16_f32 v123, v106, v107
	s_waitcnt lgkmcnt(8)
	v_mfma_f32_32x32x16_bf16 v[16:31], v[138:141], v[158:161], v[16:31]
	v_pk_add_f32 v[244:245], v[244:245], v[110:111]
	v_pk_add_f32 v[242:243], v[242:243], v[80:81]
	v_cvt_pk_bf16_f32 v124, v108, v109
	v_cvt_pk_bf16_f32 v125, v110, v111
	s_waitcnt lgkmcnt(6)
	v_mfma_f32_32x32x16_bf16 v[32:47], v[134:137], v[112:115], v[32:47]
	v_pk_add_f32 v[244:245], v[244:245], v[82:83]
	v_pk_add_f32 v[242:243], v[242:243], v[84:85]
	v_cvt_pk_bf16_f32 v118, v80, v81
	v_cvt_pk_bf16_f32 v119, v82, v83
	s_waitcnt lgkmcnt(4)
	v_mfma_f32_32x32x16_bf16 v[16:31], v[134:137], v[12:15], v[16:31]
	v_pk_add_f32 v[244:245], v[244:245], v[86:87]
	v_pk_add_f32 v[242:243], v[242:243], v[88:89]
	v_cvt_pk_bf16_f32 v120, v84, v85
	v_cvt_pk_bf16_f32 v121, v86, v87
	s_waitcnt lgkmcnt(2)
	v_mfma_f32_32x32x16_bf16 v[32:47], v[130:133], v[8:11], v[32:47]
	v_pk_add_f32 v[244:245], v[244:245], v[90:91]
	v_pk_add_f32 v[242:243], v[242:243], v[92:93]
	v_cvt_pk_bf16_f32 v114, v88, v89
	v_cvt_pk_bf16_f32 v115, v90, v91
	s_waitcnt lgkmcnt(0)
	v_mfma_f32_32x32x16_bf16 v[16:31], v[130:133], v[4:7], v[16:31]
	v_pk_add_f32 v[244:245], v[244:245], v[94:95]
	v_pk_add_f32 v[242:243], v[242:243], v[244:245]
	v_add_f32_e32 v0, v242, v243
	v_cvt_pk_bf16_f32 v116, v92, v93
	v_cvt_pk_bf16_f32 v117, v94, v95
	s_andn2_b64 vcc, exec, s[0:1]
	s_cbranch_vccnz .LBB0_585
	s_waitcnt lgkmcnt(0)
	v_lshl_add_u32 v1, v220, 2, s17
	ds_read_b128 v[4:7], v1 offset:96
	ds_read_b128 v[8:11], v1 offset:64
	ds_read_b128 v[12:15], v1 offset:32
	ds_read_b128 v[80:83], v1
	s_waitcnt lgkmcnt(3)
	v_pk_mul_f32 v[78:79], v[78:79], v[6:7]
	s_waitcnt lgkmcnt(2)
	v_pk_mul_f32 v[74:75], v[74:75], v[10:11]
	s_waitcnt lgkmcnt(1)
	v_pk_mul_f32 v[70:71], v[70:71], v[14:15]
	s_waitcnt lgkmcnt(0)
	v_pk_mul_f32 v[66:67], v[66:67], v[82:83]
	v_pk_mul_f32 v[76:77], v[76:77], v[4:5]
	v_pk_mul_f32 v[72:73], v[72:73], v[8:9]
	v_pk_mul_f32 v[68:69], v[68:69], v[12:13]
	v_pk_mul_f32 v[64:65], v[64:65], v[80:81]
	v_pk_mul_f32 v[62:63], v[62:63], v[6:7]
	v_pk_mul_f32 v[58:59], v[58:59], v[10:11]
	v_pk_mul_f32 v[54:55], v[54:55], v[14:15]
	v_pk_mul_f32 v[50:51], v[50:51], v[82:83]
	v_pk_mul_f32 v[60:61], v[60:61], v[4:5]
	v_pk_mul_f32 v[56:57], v[56:57], v[8:9]
	v_pk_mul_f32 v[52:53], v[52:53], v[12:13]
	v_pk_mul_f32 v[48:49], v[48:49], v[80:81]
	v_pk_mul_f32 v[46:47], v[46:47], v[6:7]
	v_pk_mul_f32 v[42:43], v[42:43], v[10:11]
	v_pk_mul_f32 v[38:39], v[38:39], v[14:15]
	v_pk_mul_f32 v[34:35], v[34:35], v[82:83]
	v_pk_mul_f32 v[44:45], v[44:45], v[4:5]
	v_pk_mul_f32 v[40:41], v[40:41], v[8:9]
	v_pk_mul_f32 v[36:37], v[36:37], v[12:13]
	v_pk_mul_f32 v[32:33], v[32:33], v[80:81]
	v_pk_mul_f32 v[30:31], v[30:31], v[6:7]
	v_pk_mul_f32 v[26:27], v[26:27], v[10:11]
	v_pk_mul_f32 v[22:23], v[22:23], v[14:15]
	v_pk_mul_f32 v[18:19], v[18:19], v[82:83]
	v_pk_mul_f32 v[28:29], v[28:29], v[4:5]
	v_pk_mul_f32 v[24:25], v[24:25], v[8:9]
	v_pk_mul_f32 v[20:21], v[20:21], v[12:13]
	v_pk_mul_f32 v[16:17], v[16:17], v[80:81]

.LBB0_595:
	s_waitcnt lgkmcnt(14)
	v_mfma_f32_32x32x16_bf16 v[64:79], v[142:145], v[186:189], v[64:79]
	ds_read_b64_tr_b16 v[192:193], v118 offset:32768
	ds_read_b64_tr_b16 v[194:195], v118 offset:33280
	v_exp_f32_e32 v96, v96
	v_exp_f32_e32 v97, v97
	v_exp_f32_e32 v98, v98
	v_exp_f32_e32 v99, v99
	s_waitcnt lgkmcnt(14)
	v_mfma_f32_32x32x16_bf16 v[48:63], v[142:145], v[166:169], v[48:63]
	ds_read_b64_tr_b16 v[230:231], v118 offset:36864
	ds_read_b64_tr_b16 v[232:233], v118 offset:37376
	v_exp_f32_e32 v100, v100
	v_exp_f32_e32 v101, v101
	v_exp_f32_e32 v102, v102
	v_exp_f32_e32 v103, v103
	v_add_u32_e32 v186, s23, v224
	ds_read_b128 v[166:169], v186
	ds_read_b128 v[162:165], v186 offset:512
	s_waitcnt lgkmcnt(14)
	v_mfma_f32_32x32x16_bf16 v[64:79], v[138:141], v[182:185], v[64:79]
	ds_read_b64_tr_b16 v[182:183], v118 offset:33792
	ds_read_b64_tr_b16 v[184:185], v118 offset:34304
	v_exp_f32_e32 v104, v104
	v_exp_f32_e32 v105, v105
	v_exp_f32_e32 v106, v106
	v_exp_f32_e32 v107, v107
	ds_read_b128 v[174:177], v186 offset:2048
	ds_read_b128 v[170:173], v186 offset:2560
	v_mfma_f32_32x32x16_bf16 v[48:63], v[138:141], v[178:181], v[48:63]
	ds_read_b64_tr_b16 v[178:179], v118 offset:37888
	ds_read_b64_tr_b16 v[180:181], v118 offset:38400
	v_exp_f32_e32 v108, v108
	v_exp_f32_e32 v109, v109
	v_exp_f32_e32 v110, v110
	v_exp_f32_e32 v111, v111
	s_waitcnt lgkmcnt(14)
	v_mfma_f32_32x32x16_bf16 v[64:79], v[134:137], v[112:115], v[64:79]
	ds_read_b64_tr_b16 v[112:113], v118 offset:34816
	ds_read_b64_tr_b16 v[114:115], v118 offset:35328
	v_exp_f32_e32 v80, v80
	v_exp_f32_e32 v81, v81
	v_exp_f32_e32 v82, v82
	v_exp_f32_e32 v83, v83
	v_mfma_f32_32x32x16_bf16 v[48:63], v[134:137], v[12:15], v[48:63]
	ds_read_b64_tr_b16 v[12:13], v118 offset:38912
	ds_read_b64_tr_b16 v[14:15], v118 offset:39424
	v_exp_f32_e32 v84, v84
	v_exp_f32_e32 v85, v85
	v_exp_f32_e32 v86, v86
	v_exp_f32_e32 v87, v87
	v_mfma_f32_32x32x16_bf16 v[64:79], v[130:133], v[8:11], v[64:79]
	ds_read_b64_tr_b16 v[8:9], v118 offset:35840
	ds_read_b64_tr_b16 v[10:11], v118 offset:36352
	v_exp_f32_e32 v88, v88
	v_exp_f32_e32 v89, v89
	v_exp_f32_e32 v90, v90
	v_exp_f32_e32 v91, v91
	s_waitcnt lgkmcnt(14)
	v_mfma_f32_32x32x16_bf16 v[48:63], v[130:133], v[4:7], v[48:63]
	ds_read_b64_tr_b16 v[4:5], v118 offset:39936
	ds_read_b64_tr_b16 v[6:7], v118 offset:40448
	v_exp_f32_e32 v92, v92
	v_exp_f32_e32 v93, v93
	v_exp_f32_e32 v94, v94
	v_exp_f32_e32 v95, v95
	v_mfma_f32_32x32x16_bf16 v[32:47], v[142:145], v[192:195], v[32:47]
	v_pk_add_f32 v[242:243], v[96:97], v[100:101]
	v_cvt_pk_bf16_f32 v126, v96, v97
	v_cvt_pk_bf16_f32 v127, v98, v99
	v_mfma_f32_32x32x16_bf16 v[16:31], v[142:145], v[230:233], v[16:31]
	v_pk_add_f32 v[244:245], v[98:99], v[102:103]
	v_pk_add_f32 v[242:243], v[242:243], v[104:105]
	v_cvt_pk_bf16_f32 v128, v100, v101
	v_cvt_pk_bf16_f32 v129, v102, v103
	s_waitcnt lgkmcnt(12)
	v_mfma_f32_32x32x16_bf16 v[32:47], v[138:141], v[182:185], v[32:47]
	v_pk_add_f32 v[244:245], v[244:245], v[106:107]
	v_pk_add_f32 v[242:243], v[242:243], v[108:109]
	v_cvt_pk_bf16_f32 v122, v104, v105
	v_cvt_pk_bf16_f32 v123, v106, v107
	s_waitcnt lgkmcnt(8)
	v_mfma_f32_32x32x16_bf16 v[16:31], v[138:141], v[178:181], v[16:31]
	v_pk_add_f32 v[244:245], v[244:245], v[110:111]
	v_pk_add_f32 v[242:243], v[242:243], v[80:81]
	v_cvt_pk_bf16_f32 v124, v108, v109
	v_cvt_pk_bf16_f32 v125, v110, v111
	s_waitcnt lgkmcnt(6)
	v_mfma_f32_32x32x16_bf16 v[32:47], v[134:137], v[112:115], v[32:47]
	v_pk_add_f32 v[244:245], v[244:245], v[82:83]
	v_pk_add_f32 v[242:243], v[242:243], v[84:85]
	v_cvt_pk_bf16_f32 v118, v80, v81
	v_cvt_pk_bf16_f32 v119, v82, v83
	s_waitcnt lgkmcnt(4)
	v_mfma_f32_32x32x16_bf16 v[16:31], v[134:137], v[12:15], v[16:31]
	v_pk_add_f32 v[244:245], v[244:245], v[86:87]
	v_pk_add_f32 v[242:243], v[242:243], v[88:89]
	v_cvt_pk_bf16_f32 v120, v84, v85
	v_cvt_pk_bf16_f32 v121, v86, v87
	s_waitcnt lgkmcnt(2)
	v_mfma_f32_32x32x16_bf16 v[32:47], v[130:133], v[8:11], v[32:47]
	v_pk_add_f32 v[244:245], v[244:245], v[90:91]
	v_pk_add_f32 v[242:243], v[242:243], v[92:93]
	v_cvt_pk_bf16_f32 v114, v88, v89
	v_cvt_pk_bf16_f32 v115, v90, v91
	s_waitcnt lgkmcnt(0)
	v_mfma_f32_32x32x16_bf16 v[16:31], v[130:133], v[4:7], v[16:31]
	v_pk_add_f32 v[244:245], v[244:245], v[94:95]
	v_pk_add_f32 v[242:243], v[242:243], v[244:245]
	v_add_f32_e32 v113, v242, v243
	v_cvt_pk_bf16_f32 v116, v92, v93
	v_cvt_pk_bf16_f32 v117, v94, v95
	s_mov_b64 s[10:11], -1
	s_and_b64 vcc, exec, s[4:5]
	s_cbranch_vccz .LBB0_616
	s_waitcnt vmcnt(0) lgkmcnt(0)
	s_barrier
	s_cbranch_execz .LBB0_617

.LBB0_610:
	s_waitcnt lgkmcnt(14)
	v_mfma_f32_32x32x16_bf16 v[48:63], v[122:125], v[182:185], v[48:63]
	ds_read_b64_tr_b16 v[182:183], v130 offset:37888
	ds_read_b64_tr_b16 v[184:185], v130 offset:38400
	v_exp_f32_e32 v108, v108
	v_exp_f32_e32 v109, v109
	v_exp_f32_e32 v110, v110
	v_exp_f32_e32 v111, v111
	s_waitcnt lgkmcnt(14)
	v_mfma_f32_32x32x16_bf16 v[64:79], v[118:121], v[178:181], v[64:79]
	ds_read_b64_tr_b16 v[178:179], v130 offset:34816
	ds_read_b64_tr_b16 v[180:181], v130 offset:35328
	v_exp_f32_e32 v80, v80
	v_exp_f32_e32 v81, v81
	v_exp_f32_e32 v82, v82
	v_exp_f32_e32 v83, v83
	s_waitcnt lgkmcnt(14)
	v_mfma_f32_32x32x16_bf16 v[48:63], v[118:121], v[12:15], v[48:63]
	ds_read_b64_tr_b16 v[12:13], v130 offset:38912
	ds_read_b64_tr_b16 v[14:15], v130 offset:39424
	v_exp_f32_e32 v84, v84
	v_exp_f32_e32 v85, v85
	v_exp_f32_e32 v86, v86
	v_exp_f32_e32 v87, v87
	s_waitcnt lgkmcnt(14)
	v_mfma_f32_32x32x16_bf16 v[64:79], v[114:117], v[8:11], v[64:79]
	ds_read_b64_tr_b16 v[8:9], v130 offset:35840
	ds_read_b64_tr_b16 v[10:11], v130 offset:36352
	v_exp_f32_e32 v88, v88
	v_exp_f32_e32 v89, v89
	v_exp_f32_e32 v90, v90
	v_exp_f32_e32 v91, v91
	s_waitcnt lgkmcnt(14)
	v_mfma_f32_32x32x16_bf16 v[48:63], v[114:117], v[4:7], v[48:63]
	ds_read_b64_tr_b16 v[4:5], v130 offset:39936
	ds_read_b64_tr_b16 v[6:7], v130 offset:40448
	v_exp_f32_e32 v92, v92
	v_exp_f32_e32 v93, v93
	v_exp_f32_e32 v94, v94
	v_exp_f32_e32 v95, v95
	s_waitcnt lgkmcnt(14)
	v_mfma_f32_32x32x16_bf16 v[32:47], v[126:129], v[194:197], v[32:47]
	v_pk_add_f32 v[242:243], v[96:97], v[100:101]
	v_cvt_pk_bf16_f32 v142, v96, v97
	v_cvt_pk_bf16_f32 v143, v98, v99
	s_waitcnt lgkmcnt(12)
	v_mfma_f32_32x32x16_bf16 v[16:31], v[126:129], v[190:193], v[16:31]
	v_pk_add_f32 v[244:245], v[98:99], v[102:103]
	v_pk_add_f32 v[242:243], v[242:243], v[104:105]
	v_cvt_pk_bf16_f32 v144, v100, v101
	v_cvt_pk_bf16_f32 v145, v102, v103
	s_waitcnt lgkmcnt(10)
	v_mfma_f32_32x32x16_bf16 v[32:47], v[122:125], v[186:189], v[32:47]
	v_pk_add_f32 v[244:245], v[244:245], v[106:107]
	v_pk_add_f32 v[242:243], v[242:243], v[108:109]
	v_cvt_pk_bf16_f32 v138, v104, v105
	v_cvt_pk_bf16_f32 v139, v106, v107
	s_waitcnt lgkmcnt(8)
	v_mfma_f32_32x32x16_bf16 v[16:31], v[122:125], v[182:185], v[16:31]
	v_pk_add_f32 v[244:245], v[244:245], v[110:111]
	v_pk_add_f32 v[242:243], v[242:243], v[80:81]
	v_cvt_pk_bf16_f32 v140, v108, v109
	v_cvt_pk_bf16_f32 v141, v110, v111
	s_waitcnt lgkmcnt(6)
	v_mfma_f32_32x32x16_bf16 v[32:47], v[118:121], v[178:181], v[32:47]
	v_pk_add_f32 v[244:245], v[244:245], v[82:83]
	v_pk_add_f32 v[242:243], v[242:243], v[84:85]
	v_cvt_pk_bf16_f32 v134, v80, v81
	v_cvt_pk_bf16_f32 v135, v82, v83
	s_waitcnt lgkmcnt(4)
	v_mfma_f32_32x32x16_bf16 v[16:31], v[118:121], v[12:15], v[16:31]
	v_pk_add_f32 v[244:245], v[244:245], v[86:87]
	v_pk_add_f32 v[242:243], v[242:243], v[88:89]
	v_cvt_pk_bf16_f32 v136, v84, v85
	v_cvt_pk_bf16_f32 v137, v86, v87
	s_waitcnt lgkmcnt(2)
	v_mfma_f32_32x32x16_bf16 v[32:47], v[114:117], v[8:11], v[32:47]
	v_pk_add_f32 v[244:245], v[244:245], v[90:91]
	v_pk_add_f32 v[242:243], v[242:243], v[92:93]
	v_cvt_pk_bf16_f32 v130, v88, v89
	v_cvt_pk_bf16_f32 v131, v90, v91
	s_waitcnt lgkmcnt(0)
	v_mfma_f32_32x32x16_bf16 v[16:31], v[114:117], v[4:7], v[16:31]
	v_pk_add_f32 v[244:245], v[244:245], v[94:95]
	v_pk_add_f32 v[242:243], v[242:243], v[244:245]
	v_add_f32_e32 v4, v242, v243
	v_cvt_pk_bf16_f32 v132, v92, v93
	v_cvt_pk_bf16_f32 v133, v94, v95
	s_mov_b64 s[4:5], -1
	s_and_b64 vcc, exec, s[8:9]
	s_cbranch_vccz .LBB0_618
	s_waitcnt vmcnt(0) lgkmcnt(0)
	s_barrier
	s_cbranch_execz .LBB0_619
